# prep also touches the lines holding the kernel descriptors of the following launches (rodata below the entry); otherwise v23
# speedup vs baseline: 1.0108x; 1.0108x over previous
.Lprep_pf2:
	s_mov_b64 exec, s[20:21]
	v_subrev_u32_e32 v30, 0x300, v0
	v_cmp_gt_u32_e32 vcc, 64, v30
	s_and_saveexec_b64 s[20:21], vcc
	s_cbranch_execz .Lprep_pf3
	s_sub_u32 s24, s22, 0x1300
	s_subb_u32 s25, s23, 0
	v_lshlrev_b32_e32 v30, 4, v30
	global_load_dwordx4 v[32:35], v30, s[24:25]
